# conversion bf16 tails: four LDS reads per store issued together (8 instead of 32 dependent LDS round trips per item) in the three mixer-phase instances
# baseline (speedup 1.0000x reference)
.LBB0_1026:
	s_lshr_b32 s7, s62, 9
	s_mul_hi_u32 s58, s7, 0x2302303
	s_mul_i32 s55, s58, 0xea00
	s_sub_i32 s52, s78, s55
	s_add_i32 s29, s82, s28
	s_cmpk_eq_i32 s26, 0x1c0
	s_cselect_b64 s[56:57], -1, 0
	s_add_i32 s53, s67, s28
	s_lshr_b32 s7, s29, 9
	s_add_i32 s54, s53, s52
	s_mul_hi_u32 s8, s7, 0x2302303
	s_cmpk_gt_i32 s54, 0x4dff
	s_mov_b64 s[40:41], -1
	s_cbranch_scc0 .LBB0_1112
	s_cmpk_gt_u32 s54, 0x59ff
	s_cbranch_scc0 .LBB0_1109
	s_mul_i32 s58, s58, 0x75000
	s_cmpk_gt_u32 s54, 0x69ff
	s_cbranch_scc0 .LBB0_1106
	s_cmpk_gt_u32 s54, 0xa9ff
	s_cbranch_scc0 .LBB0_1031
	s_sub_i32 s7, s62, s55
	s_and_b32 s40, s7, 0xfe00
	s_load_dwordx2 s[50:51], s[0:1], 0x68
	s_add_i32 s49, s40, 0xffff5600
	s_add_i32 s41, s40, 0xffff563c
	s_add_i32 s44, s40, 0xffff5638
	s_add_i32 s45, s40, 0xffff5634
	s_add_i32 s46, s40, 0xffff5630
	s_add_i32 s47, s40, 0xffff562c
	s_add_i32 s48, s40, 0xffff5628
	s_add_i32 s7, s40, 0xffff5624
	s_add_i32 s10, s40, 0xffff5620
	s_add_i32 s11, s40, 0xffff561c
	s_add_i32 s59, s40, 0xffff5618
	s_add_i32 s77, s40, 0xffff5614
	s_add_i32 s89, s40, 0xffff5610
	s_add_i32 s91, s40, 0xffff560c
	s_add_i32 vcc_lo, s40, 0xffff5608
	s_add_i32 vcc_hi, s40, 0xffff5604
	s_add_i32 s40, s26, s49
	s_lshl_b64 s[42:43], s[8:9], 27
	s_add_u32 s42, s71, s42
	s_addc_u32 s43, s23, s43
	s_lshl_b64 s[60:61], s[8:9], 28
	s_waitcnt lgkmcnt(0)
	s_add_u32 s50, s50, s60
	v_add_u32_e32 v8, s26, v67
	s_addc_u32 s51, s51, s61
	v_add_u32_e32 v2, s49, v8
	s_lshl_b32 s49, s63, 2
	s_add_u32 s50, s50, s49
	s_addc_u32 s51, s51, 0
	v_lshlrev_b32_e32 v0, 2, v66
	v_ashrrev_i32_e32 v3, 31, v2
	v_lshl_add_u64 v[6:7], s[50:51], 0, v[0:1]
	v_lshlrev_b64 v[2:3], 14, v[2:3]
	v_lshl_add_u64 v[2:3], v[6:7], 0, v[2:3]
	global_load_dwordx4 v[38:41], v[2:3], off nt
	v_add_u32_e32 v2, vcc_hi, v8
	v_ashrrev_i32_e32 v3, 31, v2
	v_lshlrev_b64 v[2:3], 14, v[2:3]
	v_lshl_add_u64 v[2:3], v[6:7], 0, v[2:3]
	global_load_dwordx4 v[42:45], v[2:3], off nt
	v_add_u32_e32 v2, vcc_lo, v8
	v_ashrrev_i32_e32 v3, 31, v2
	v_lshlrev_b64 v[2:3], 14, v[2:3]
	v_lshl_add_u64 v[2:3], v[6:7], 0, v[2:3]
	global_load_dwordx4 v[46:49], v[2:3], off nt
	v_add_u32_e32 v2, s91, v8
	v_ashrrev_i32_e32 v3, 31, v2
	v_lshlrev_b64 v[2:3], 14, v[2:3]
	v_lshl_add_u64 v[2:3], v[6:7], 0, v[2:3]
	global_load_dwordx4 v[50:53], v[2:3], off nt
	v_add_u32_e32 v2, s89, v8
	v_ashrrev_i32_e32 v3, 31, v2
	v_lshlrev_b64 v[2:3], 14, v[2:3]
	v_lshl_add_u64 v[2:3], v[6:7], 0, v[2:3]
	global_load_dwordx4 v[54:57], v[2:3], off nt
	v_add_u32_e32 v2, s77, v8
	v_ashrrev_i32_e32 v3, 31, v2
	v_lshlrev_b64 v[2:3], 14, v[2:3]
	v_lshl_add_u64 v[2:3], v[6:7], 0, v[2:3]
	global_load_dwordx4 v[62:65], v[2:3], off nt
	v_add_u32_e32 v2, s59, v8
	v_ashrrev_i32_e32 v3, 31, v2
	v_lshlrev_b64 v[2:3], 14, v[2:3]
	v_lshl_add_u64 v[2:3], v[6:7], 0, v[2:3]
	global_load_dwordx4 v[58:61], v[2:3], off nt
	v_add_u32_e32 v2, s11, v8
	v_ashrrev_i32_e32 v3, 31, v2
	v_lshlrev_b64 v[2:3], 14, v[2:3]
	v_lshl_add_u64 v[2:3], v[6:7], 0, v[2:3]
	global_load_dwordx4 v[34:37], v[2:3], off nt
	v_add_u32_e32 v2, s10, v8
	v_ashrrev_i32_e32 v3, 31, v2
	v_lshlrev_b64 v[2:3], 14, v[2:3]
	v_lshl_add_u64 v[2:3], v[6:7], 0, v[2:3]
	global_load_dwordx4 v[30:33], v[2:3], off nt
	v_add_u32_e32 v2, s7, v8
	v_ashrrev_i32_e32 v3, 31, v2
	v_lshlrev_b64 v[2:3], 14, v[2:3]
	v_lshl_add_u64 v[2:3], v[6:7], 0, v[2:3]
	global_load_dwordx4 v[26:29], v[2:3], off nt
	v_add_u32_e32 v2, s48, v8
	v_ashrrev_i32_e32 v3, 31, v2
	v_lshlrev_b64 v[2:3], 14, v[2:3]
	v_lshl_add_u64 v[2:3], v[6:7], 0, v[2:3]
	global_load_dwordx4 v[22:25], v[2:3], off nt
	v_add_u32_e32 v2, s47, v8
	v_ashrrev_i32_e32 v3, 31, v2
	v_lshlrev_b64 v[2:3], 14, v[2:3]
	v_lshl_add_u64 v[2:3], v[6:7], 0, v[2:3]
	global_load_dwordx4 v[18:21], v[2:3], off nt
	v_add_u32_e32 v2, s46, v8
	v_ashrrev_i32_e32 v3, 31, v2
	v_lshlrev_b64 v[2:3], 14, v[2:3]
	v_lshl_add_u64 v[2:3], v[6:7], 0, v[2:3]
	global_load_dwordx4 v[14:17], v[2:3], off nt
	v_add_u32_e32 v2, s45, v8
	v_ashrrev_i32_e32 v3, 31, v2
	v_lshlrev_b64 v[2:3], 14, v[2:3]
	v_lshl_add_u64 v[2:3], v[6:7], 0, v[2:3]
	global_load_dwordx4 v[10:13], v[2:3], off nt
	v_add_u32_e32 v2, s44, v8
	v_add_u32_e32 v8, s41, v8
	v_ashrrev_i32_e32 v3, 31, v2
	v_ashrrev_i32_e32 v9, 31, v8
	v_lshlrev_b64 v[2:3], 14, v[2:3]
	v_lshlrev_b64 v[8:9], 14, v[8:9]
	v_lshl_add_u64 v[2:3], v[6:7], 0, v[2:3]
	v_lshl_add_u64 v[6:7], v[6:7], 0, v[8:9]
	global_load_dwordx4 v[2:5], v[2:3], off nt
	s_mov_b32 s41, s9
	global_load_dwordx4 v[6:9], v[6:7], off nt
	s_waitcnt vmcnt(15)
	v_cvt_pk_bf16_f32 v0, v38, v38
	s_lshl_b64 s[10:11], s[40:41], 1
	v_lshlrev_b32_e32 v108, 16, v0
	ds_write_b32 v69, v108
	v_cvt_pk_bf16_f32 v0, v39, v39
	v_pk_fma_f32 v[38:39], v[38:39], 0, v[106:107] op_sel_hi:[1,0,1]
	v_lshlrev_b32_e32 v109, 16, v0
	ds_write_b32 v69, v109 offset:4
	v_cvt_pk_bf16_f32 v0, v40, v40
	v_pk_add_f32 v[108:109], v[100:101], v[108:109]
	v_lshlrev_b32_e32 v110, 16, v0
	ds_write_b32 v69, v110 offset:8
	v_cvt_pk_bf16_f32 v0, v41, v41
	s_waitcnt vmcnt(14)
	v_pk_fma_f32 v[38:39], v[42:43], 0, v[38:39] op_sel_hi:[1,0,1]
	v_lshlrev_b32_e32 v111, 16, v0
	ds_write_b32 v69, v111 offset:12
	v_cvt_pk_bf16_f32 v0, v42, v42
	v_pk_add_f32 v[110:111], v[102:103], v[110:111]
	v_lshlrev_b32_e32 v114, 16, v0
	ds_write_b32 v69, v114 offset:1040
	v_cvt_pk_bf16_f32 v0, v43, v43
	s_waitcnt vmcnt(13)
	v_pk_fma_f32 v[38:39], v[46:47], 0, v[38:39] op_sel_hi:[1,0,1]
	v_lshlrev_b32_e32 v115, 16, v0
	ds_write_b32 v69, v115 offset:1044
	v_pk_add_f32 v[108:109], v[108:109], v[114:115]
	v_cvt_pk_bf16_f32 v0, v44, v44
	s_waitcnt vmcnt(11)
	v_mul_f32_e32 v113, 0, v55
	v_lshlrev_b32_e32 v114, 16, v0
	ds_write_b32 v69, v114 offset:1048
	v_cvt_pk_bf16_f32 v0, v45, v45
	v_pk_fma_f32 v[38:39], v[50:51], 0, v[38:39] op_sel_hi:[1,0,1]
	v_lshlrev_b32_e32 v115, 16, v0
	ds_write_b32 v69, v115 offset:1052
	v_pk_add_f32 v[110:111], v[110:111], v[114:115]
	v_cvt_pk_bf16_f32 v0, v46, v46
	v_pk_fma_f32 v[40:41], v[40:41], 0, v[104:105] op_sel_hi:[1,0,1]
	v_lshlrev_b32_e32 v114, 16, v0
	ds_write_b32 v69, v114 offset:2080
	v_cvt_pk_bf16_f32 v0, v47, v47
	v_pk_fma_f32 v[40:41], v[44:45], 0, v[40:41] op_sel_hi:[1,0,1]
	v_lshlrev_b32_e32 v115, 16, v0
	ds_write_b32 v69, v115 offset:2084
	v_pk_add_f32 v[108:109], v[108:109], v[114:115]
	v_cvt_pk_bf16_f32 v0, v48, v48
	v_pk_fma_f32 v[40:41], v[48:49], 0, v[40:41] op_sel_hi:[1,0,1]
	v_lshlrev_b32_e32 v114, 16, v0
	ds_write_b32 v69, v114 offset:2088
	v_cvt_pk_bf16_f32 v0, v49, v49
	v_pk_fma_f32 v[40:41], v[52:53], 0, v[40:41] op_sel_hi:[1,0,1]
	v_lshlrev_b32_e32 v115, 16, v0
	ds_write_b32 v69, v115 offset:2092
	v_pk_add_f32 v[110:111], v[110:111], v[114:115]
	v_cvt_pk_bf16_f32 v0, v50, v50
	s_waitcnt vmcnt(7)
	v_mov_b32_e32 v49, v30
	v_lshlrev_b32_e32 v114, 16, v0
	ds_write_b32 v69, v114 offset:3120
	v_cvt_pk_bf16_f32 v0, v51, v51
	s_waitcnt vmcnt(6)
	v_mov_b32_e32 v48, v26
	v_lshlrev_b32_e32 v115, 16, v0
	ds_write_b32 v69, v115 offset:3124
	v_pk_add_f32 v[108:109], v[108:109], v[114:115]
	v_cvt_pk_bf16_f32 v0, v52, v52
	s_waitcnt vmcnt(4)
	v_mov_b32_e32 v52, v18
	v_lshlrev_b32_e32 v114, 16, v0
	ds_write_b32 v69, v114 offset:3128
	v_cvt_pk_bf16_f32 v0, v53, v53
	v_mov_b32_e32 v53, v22
	v_lshlrev_b32_e32 v115, 16, v0
	ds_write_b32 v69, v115 offset:3132
	v_pk_add_f32 v[110:111], v[110:111], v[114:115]
	v_cvt_pk_bf16_f32 v0, v54, v54
	v_pk_mul_f32 v[128:129], v[52:53], 0 op_sel_hi:[1,0]
	v_lshlrev_b32_e32 v114, 16, v0
	ds_write_b32 v69, v114 offset:4160
	v_cvt_pk_bf16_f32 v0, v55, v55
	v_mul_f32_e32 v130, 0, v19
	v_lshlrev_b32_e32 v115, 16, v0
	ds_write_b32 v69, v115 offset:4164
	v_pk_add_f32 v[116:117], v[108:109], v[114:115]
	v_cvt_pk_bf16_f32 v0, v56, v56
	s_waitcnt vmcnt(0)
	v_mov_b32_e32 v136, v6
	v_lshlrev_b32_e32 v108, 16, v0
	ds_write_b32 v69, v108 offset:4168
	v_cvt_pk_bf16_f32 v0, v57, v57
	v_mov_b32_e32 v137, v2
	v_lshlrev_b32_e32 v109, 16, v0
	ds_write_b32 v69, v109 offset:4172
	v_cvt_pk_bf16_f32 v0, v62, v62
	v_pk_add_f32 v[108:109], v[110:111], v[108:109]
	v_lshlrev_b32_e32 v118, 16, v0
	v_mov_b32_e32 v110, v62
	v_mov_b32_e32 v111, v54
	ds_write_b32 v69, v118 offset:5200
	v_cvt_pk_bf16_f32 v0, v63, v63
	v_pk_mul_f32 v[110:111], v[110:111], 0 op_sel_hi:[1,0]
	v_lshlrev_b32_e32 v119, 16, v0
	ds_write_b32 v69, v119 offset:5204
	v_cvt_pk_bf16_f32 v0, v64, v64
	v_mov_b32_e32 v112, v111
	v_lshlrev_b32_e32 v62, 16, v0
	v_mul_f32_e32 v111, 0, v63
	ds_write_b32 v69, v62 offset:5208
	v_cvt_pk_bf16_f32 v0, v65, v65
	v_pk_add_f32 v[112:113], v[112:113], v[38:39]
	v_lshlrev_b32_e32 v63, 16, v0
	ds_write_b32 v69, v63 offset:5212
	v_cvt_pk_bf16_f32 v0, v58, v58
	v_mov_b32_e32 v38, v64
	v_lshlrev_b32_e32 v120, 16, v0
	v_mov_b32_e32 v39, v56
	v_mov_b32_e32 v56, v65
	ds_write_b32 v69, v120 offset:6240
	v_cvt_pk_bf16_f32 v0, v59, v59
	v_pk_mul_f32 v[38:39], v[38:39], 0 op_sel_hi:[1,0]
	v_lshlrev_b32_e32 v121, 16, v0
	v_pk_mul_f32 v[42:43], v[56:57], 0 op_sel_hi:[1,0]
	ds_write_b32 v69, v121 offset:6244
	v_cvt_pk_bf16_f32 v0, v60, v60
	v_mov_b32_e32 v44, v39
	v_lshlrev_b32_e32 v64, 16, v0
	v_mov_b32_e32 v45, v43
	ds_write_b32 v69, v64 offset:6248
	v_cvt_pk_bf16_f32 v0, v61, v61
	v_pk_add_f32 v[40:41], v[44:45], v[40:41]
	v_lshlrev_b32_e32 v65, 16, v0
	ds_write_b32 v69, v65 offset:6252
	v_cvt_pk_bf16_f32 v0, v34, v34
	v_mov_b32_e32 v44, v34
	v_lshlrev_b32_e32 v34, 16, v0
	v_mov_b32_e32 v45, v58
	v_mul_f32_e32 v39, 0, v35
	v_mov_b32_e32 v56, v10
	v_mov_b32_e32 v57, v14
	ds_write_b32 v69, v34 offset:7280
	v_cvt_pk_bf16_f32 v0, v35, v35
	v_pk_mul_f32 v[122:123], v[44:45], 0 op_sel_hi:[1,0]
	v_lshlrev_b32_e32 v35, 16, v0
	v_mov_b32_e32 v44, v36
	v_pk_mul_f32 v[132:133], v[56:57], 0 op_sel_hi:[1,0]
	v_mul_f32_e32 v134, 0, v11
	v_pk_mul_f32 v[136:137], v[136:137], 0 op_sel_hi:[1,0]
	ds_write_b32 v69, v35 offset:7284
	v_cvt_pk_bf16_f32 v0, v36, v36
	v_mul_f32_e32 v36, 0, v7
	v_mov_b32_e32 v126, v129
	v_mov_b32_e32 v129, v130
	v_mov_b32_e32 v130, v133
	v_mov_b32_e32 v133, v134
	v_mov_b32_e32 v134, v137
	v_mov_b32_e32 v137, v36
	v_lshlrev_b32_e32 v36, 16, v0
	v_mov_b32_e32 v45, v60
	v_mov_b32_e32 v60, v37
	ds_write_b32 v69, v36 offset:7288
	v_cvt_pk_bf16_f32 v0, v37, v37
	v_pk_mul_f32 v[46:47], v[60:61], 0 op_sel_hi:[1,0]
	v_lshlrev_b32_e32 v37, 16, v0
	ds_write_b32 v69, v37 offset:7292
	v_cvt_pk_bf16_f32 v0, v30, v30
	v_mul_f32_e32 v61, 0, v31
	v_lshlrev_b32_e32 v30, 16, v0
	ds_write_b32 v69, v30 offset:8320
	v_cvt_pk_bf16_f32 v0, v31, v31
	v_pk_mul_f32 v[124:125], v[48:49], 0 op_sel_hi:[1,0]
	v_lshlrev_b32_e32 v31, 16, v0
	v_mov_b32_e32 v49, v32
	ds_write_b32 v69, v31 offset:8324
	v_cvt_pk_bf16_f32 v0, v32, v32
	v_mov_b32_e32 v51, v33
	v_lshlrev_b32_e32 v32, 16, v0
	ds_write_b32 v69, v32 offset:8328
	v_cvt_pk_bf16_f32 v0, v33, v33
	v_mul_f32_e32 v43, 0, v27
	v_lshlrev_b32_e32 v33, 16, v0
	ds_write_b32 v69, v33 offset:8332
	v_cvt_pk_bf16_f32 v0, v26, v26
	v_mov_b32_e32 v48, v28
	v_lshlrev_b32_e32 v26, 16, v0
	ds_write_b32 v69, v26 offset:9360
	v_cvt_pk_bf16_f32 v0, v27, v27
	v_mov_b32_e32 v50, v29
	v_lshlrev_b32_e32 v27, 16, v0
	ds_write_b32 v69, v27 offset:9364
	v_cvt_pk_bf16_f32 v0, v28, v28
	v_mul_f32_e32 v127, 0, v23
	v_lshlrev_b32_e32 v28, 16, v0
	ds_write_b32 v69, v28 offset:9368
	v_cvt_pk_bf16_f32 v0, v29, v29
	v_mov_b32_e32 v53, v24
	v_lshlrev_b32_e32 v29, 16, v0
	ds_write_b32 v69, v29 offset:9372
	v_cvt_pk_bf16_f32 v0, v22, v22
	v_mov_b32_e32 v55, v25
	v_lshlrev_b32_e32 v22, 16, v0
	ds_write_b32 v69, v22 offset:10400
	v_cvt_pk_bf16_f32 v0, v23, v23
	v_mov_b32_e32 v52, v20
	v_lshlrev_b32_e32 v23, 16, v0
	ds_write_b32 v69, v23 offset:10404
	v_cvt_pk_bf16_f32 v0, v24, v24
	v_mov_b32_e32 v54, v21
	v_lshlrev_b32_e32 v24, 16, v0
	ds_write_b32 v69, v24 offset:10408
	v_cvt_pk_bf16_f32 v0, v25, v25
	v_mul_f32_e32 v131, 0, v15
	v_lshlrev_b32_e32 v25, 16, v0
	ds_write_b32 v69, v25 offset:10412
	v_cvt_pk_bf16_f32 v0, v18, v18
	v_pk_add_f32 v[116:117], v[116:117], v[118:119]
	v_lshlrev_b32_e32 v18, 16, v0
	ds_write_b32 v69, v18 offset:11440
	v_cvt_pk_bf16_f32 v0, v19, v19
	v_mov_b32_e32 v57, v16
	v_lshlrev_b32_e32 v19, 16, v0
	ds_write_b32 v69, v19 offset:11444
	v_cvt_pk_bf16_f32 v0, v20, v20
	v_pk_add_f32 v[116:117], v[116:117], v[120:121]
	v_lshlrev_b32_e32 v20, 16, v0
	ds_write_b32 v69, v20 offset:11448
	v_cvt_pk_bf16_f32 v0, v21, v21
	v_mul_f32_e32 v115, 0, v59
	v_lshlrev_b32_e32 v21, 16, v0
	ds_write_b32 v69, v21 offset:11452
	v_cvt_pk_bf16_f32 v0, v14, v14
	v_mov_b32_e32 v59, v17
	v_lshlrev_b32_e32 v14, 16, v0
	ds_write_b32 v69, v14 offset:12480
	v_cvt_pk_bf16_f32 v0, v15, v15
	v_pk_add_f32 v[116:117], v[116:117], v[34:35]
	v_lshlrev_b32_e32 v15, 16, v0
	ds_write_b32 v69, v15 offset:12484
	v_cvt_pk_bf16_f32 v0, v16, v16
	v_pk_add_f32 v[30:31], v[116:117], v[30:31]
	v_lshlrev_b32_e32 v16, 16, v0
	ds_write_b32 v69, v16 offset:12488
	v_cvt_pk_bf16_f32 v0, v17, v17
	v_pk_add_f32 v[62:63], v[108:109], v[62:63]
	v_lshlrev_b32_e32 v17, 16, v0
	ds_write_b32 v69, v17 offset:12492
	v_cvt_pk_bf16_f32 v0, v10, v10
	v_pk_add_f32 v[26:27], v[30:31], v[26:27]
	v_lshlrev_b32_e32 v10, 16, v0
	ds_write_b32 v69, v10 offset:13520
	v_cvt_pk_bf16_f32 v0, v11, v11
	v_mov_b32_e32 v56, v12
	v_lshlrev_b32_e32 v11, 16, v0
	v_pk_add_f32 v[62:63], v[62:63], v[64:65]
	v_pk_add_f32 v[22:23], v[26:27], v[22:23]
	ds_write_b32 v69, v11 offset:13524
	v_cvt_pk_bf16_f32 v0, v12, v12
	v_mov_b32_e32 v58, v13
	v_lshlrev_b32_e32 v12, 16, v0
	v_pk_add_f32 v[36:37], v[62:63], v[36:37]
	v_pk_add_f32 v[18:19], v[22:23], v[18:19]
	ds_write_b32 v69, v12 offset:13528
	v_cvt_pk_bf16_f32 v0, v13, v13
	v_pk_add_f32 v[32:33], v[36:37], v[32:33]
	v_lshlrev_b32_e32 v13, 16, v0
	v_pk_add_f32 v[14:15], v[18:19], v[14:15]
	ds_write_b32 v69, v13 offset:13532
	v_cvt_pk_bf16_f32 v0, v2, v2
	v_mul_f32_e32 v135, 0, v3
	v_lshlrev_b32_e32 v2, 16, v0
	v_pk_add_f32 v[28:29], v[32:33], v[28:29]
	v_pk_add_f32 v[10:11], v[14:15], v[10:11]
	ds_write_b32 v69, v2 offset:14560
	v_cvt_pk_bf16_f32 v0, v3, v3
	v_pk_add_f32 v[24:25], v[28:29], v[24:25]
	v_lshlrev_b32_e32 v3, 16, v0
	ds_write_b32 v69, v3 offset:14564
	v_pk_add_f32 v[2:3], v[10:11], v[2:3]
	v_cvt_pk_bf16_f32 v0, v4, v4
	v_pk_add_f32 v[20:21], v[24:25], v[20:21]
	v_lshlrev_b32_e32 v10, 16, v0
	ds_write_b32 v69, v10 offset:14568
	v_cvt_pk_bf16_f32 v0, v5, v5
	v_pk_add_f32 v[16:17], v[20:21], v[16:17]
	v_lshlrev_b32_e32 v11, 16, v0
	ds_write_b32 v69, v11 offset:14572
	v_cvt_pk_bf16_f32 v0, v6, v6
	v_pk_add_f32 v[34:35], v[110:111], v[112:113]
	v_lshlrev_b32_e32 v6, 16, v0
	v_mov_b32_e32 v114, v123
	v_pk_add_f32 v[12:13], v[16:17], v[12:13]
	ds_write_b32 v69, v6 offset:15600
	v_cvt_pk_bf16_f32 v0, v7, v7
	v_pk_add_f32 v[34:35], v[114:115], v[34:35]
	v_lshlrev_b32_e32 v7, 16, v0
	v_mov_b32_e32 v123, v39
	v_pk_add_f32 v[12:13], v[12:13], v[10:11]
	v_pk_add_f32 v[10:11], v[2:3], v[6:7]
	ds_write_b32 v69, v7 offset:15604
	v_cvt_pk_bf16_f32 v0, v8, v8
	v_pk_mul_f32 v[44:45], v[44:45], 0 op_sel_hi:[1,0]
	v_lshlrev_b32_e32 v6, 16, v0
	v_pk_add_f32 v[34:35], v[122:123], v[34:35]
	v_mov_b32_e32 v60, v125
	ds_write_b32 v69, v6 offset:15608
	v_cvt_pk_bf16_f32 v0, v9, v9
	v_mov_b32_e32 v39, v42
	v_lshlrev_b32_e32 v7, 16, v0
	v_pk_add_f32 v[34:35], v[60:61], v[34:35]
	v_mov_b32_e32 v60, v8
	v_mov_b32_e32 v61, v4
	v_pk_add_f32 v[2:3], v[12:13], v[6:7]
	ds_write_b32 v69, v7 offset:15612
	v_mov_b32_e32 v4, v9
	v_pk_add_f32 v[6:7], v[38:39], v[40:41]
	v_mov_b32_e32 v8, v45
	v_mov_b32_e32 v9, v47
	v_pk_mul_f32 v[48:49], v[48:49], 0 op_sel_hi:[1,0]
	v_pk_mul_f32 v[50:51], v[50:51], 0 op_sel_hi:[1,0]
	v_pk_add_f32 v[6:7], v[8:9], v[6:7]
	v_mov_b32_e32 v45, v46
	v_pk_add_f32 v[6:7], v[44:45], v[6:7]
	v_mov_b32_e32 v8, v49
	v_mov_b32_e32 v9, v51
	v_pk_mul_f32 v[52:53], v[52:53], 0 op_sel_hi:[1,0]
	v_pk_mul_f32 v[54:55], v[54:55], 0 op_sel_hi:[1,0]
	v_pk_add_f32 v[6:7], v[8:9], v[6:7]
	v_mov_b32_e32 v49, v50
	v_pk_add_f32 v[6:7], v[48:49], v[6:7]
	v_mov_b32_e32 v8, v53
	v_mov_b32_e32 v9, v55
	v_pk_mul_f32 v[56:57], v[56:57], 0 op_sel_hi:[1,0]
	v_pk_mul_f32 v[58:59], v[58:59], 0 op_sel_hi:[1,0]
	v_pk_add_f32 v[6:7], v[8:9], v[6:7]
	v_mov_b32_e32 v53, v54
	v_pk_add_f32 v[6:7], v[52:53], v[6:7]
	v_mov_b32_e32 v8, v57
	v_mov_b32_e32 v9, v59
	v_pk_mul_f32 v[60:61], v[60:61], 0 op_sel_hi:[1,0]
	v_pk_mul_f32 v[4:5], v[4:5], 0 op_sel_hi:[1,0]
	v_pk_add_f32 v[6:7], v[8:9], v[6:7]
	v_mov_b32_e32 v57, v58
	s_waitcnt lgkmcnt(0)
	v_pk_add_f32 v[6:7], v[56:57], v[6:7]
	v_mov_b32_e32 v8, v61
	v_mov_b32_e32 v9, v5
	s_add_u32 s10, s42, s10
	v_pk_add_f32 v[6:7], v[8:9], v[6:7]
	v_mov_b32_e32 v61, v4
	s_addc_u32 s11, s43, s11
	v_lshlrev_b32_e32 v0, 1, v68
	ds_read2_b32 v[16:17], v205 offset1:65
	v_pk_add_f32 v[4:5], v[60:61], v[6:7]
	v_lshl_add_u64 v[6:7], s[10:11], 0, v[0:1]
	ds_read2_b32 v[18:19], v205 offset0:130 offset1:195
	v_add_u32_e32 v0, 0x400, v205
	ds_read2_b32 v[20:21], v0 offset0:4 offset1:69
	ds_read2_b32 v[8:9], v0 offset0:134 offset1:199
	s_waitcnt lgkmcnt(0)
	v_cvt_pk_bf16_f32 v12, v16, v17
	v_cvt_pk_bf16_f32 v13, v18, v19
	v_cvt_pk_bf16_f32 v14, v20, v21
	v_cvt_pk_bf16_f32 v15, v8, v9
	v_lshl_add_u64 v[8:9], v[6:7], 0, v[76:77]
	global_store_dwordx4 v[8:9], v[12:15], off nt
	ds_read2_b32 v[16:17], v205 offset0:8 offset1:73
	v_mov_b32_e32 v125, v43
	ds_read2_b32 v[18:19], v205 offset0:138 offset1:203
	ds_read2_b32 v[20:21], v0 offset0:12 offset1:77
	ds_read2_b32 v[8:9], v0 offset0:142 offset1:207
	s_waitcnt lgkmcnt(0)
	v_cvt_pk_bf16_f32 v12, v16, v17
	v_cvt_pk_bf16_f32 v13, v18, v19
	v_cvt_pk_bf16_f32 v14, v20, v21
	v_cvt_pk_bf16_f32 v15, v8, v9
	v_lshl_add_u64 v[8:9], v[6:7], 0, v[78:79]
	global_store_dwordx4 v[8:9], v[12:15], off nt
	ds_read2_b32 v[16:17], v205 offset0:16 offset1:81
	v_pk_add_f32 v[34:35], v[124:125], v[34:35]
	ds_read2_b32 v[18:19], v205 offset0:146 offset1:211
	ds_read2_b32 v[20:21], v0 offset0:20 offset1:85
	ds_read2_b32 v[8:9], v0 offset0:150 offset1:215
	s_waitcnt lgkmcnt(0)
	v_cvt_pk_bf16_f32 v12, v16, v17
	v_cvt_pk_bf16_f32 v13, v18, v19
	v_cvt_pk_bf16_f32 v14, v20, v21
	v_cvt_pk_bf16_f32 v15, v8, v9
	v_lshl_add_u64 v[8:9], v[6:7], 0, v[80:81]
	global_store_dwordx4 v[8:9], v[12:15], off nt
	ds_read2_b32 v[16:17], v205 offset0:24 offset1:89
	v_pk_add_f32 v[34:35], v[126:127], v[34:35]
	ds_read2_b32 v[18:19], v205 offset0:154 offset1:219
	ds_read2_b32 v[20:21], v0 offset0:28 offset1:93
	ds_read2_b32 v[8:9], v0 offset0:158 offset1:223
	s_waitcnt lgkmcnt(0)
	v_cvt_pk_bf16_f32 v12, v16, v17
	v_cvt_pk_bf16_f32 v13, v18, v19
	v_cvt_pk_bf16_f32 v14, v20, v21
	v_cvt_pk_bf16_f32 v15, v8, v9
	v_lshl_add_u64 v[8:9], v[6:7], 0, v[82:83]
	global_store_dwordx4 v[8:9], v[12:15], off nt
	ds_read2_b32 v[16:17], v205 offset0:32 offset1:97
	v_pk_add_f32 v[34:35], v[128:129], v[34:35]
	ds_read2_b32 v[18:19], v205 offset0:162 offset1:227
	ds_read2_b32 v[20:21], v0 offset0:36 offset1:101
	ds_read2_b32 v[8:9], v0 offset0:166 offset1:231
	s_waitcnt lgkmcnt(0)
	v_cvt_pk_bf16_f32 v12, v16, v17
	v_cvt_pk_bf16_f32 v13, v18, v19
	v_cvt_pk_bf16_f32 v14, v20, v21
	v_cvt_pk_bf16_f32 v15, v8, v9
	v_lshl_add_u64 v[8:9], v[6:7], 0, v[84:85]
	global_store_dwordx4 v[8:9], v[12:15], off nt
	ds_read2_b32 v[16:17], v205 offset0:40 offset1:105
	v_pk_add_f32 v[34:35], v[130:131], v[34:35]
	ds_read2_b32 v[18:19], v205 offset0:170 offset1:235
	ds_read2_b32 v[20:21], v0 offset0:44 offset1:109
	ds_read2_b32 v[8:9], v0 offset0:174 offset1:239
	s_waitcnt lgkmcnt(0)
	v_cvt_pk_bf16_f32 v12, v16, v17
	v_cvt_pk_bf16_f32 v13, v18, v19
	v_cvt_pk_bf16_f32 v14, v20, v21
	v_cvt_pk_bf16_f32 v15, v8, v9
	v_lshl_add_u64 v[8:9], v[6:7], 0, v[86:87]
	global_store_dwordx4 v[8:9], v[12:15], off nt
	ds_read2_b32 v[16:17], v205 offset0:48 offset1:113
	v_pk_add_f32 v[34:35], v[132:133], v[34:35]
	ds_read2_b32 v[18:19], v205 offset0:178 offset1:243
	ds_read2_b32 v[20:21], v0 offset0:52 offset1:117
	ds_read2_b32 v[8:9], v0 offset0:182 offset1:247
	s_waitcnt lgkmcnt(0)
	v_cvt_pk_bf16_f32 v12, v16, v17
	v_cvt_pk_bf16_f32 v13, v18, v19
	v_cvt_pk_bf16_f32 v14, v20, v21
	v_cvt_pk_bf16_f32 v15, v8, v9
	v_lshl_add_u64 v[8:9], v[6:7], 0, v[88:89]
	global_store_dwordx4 v[8:9], v[12:15], off nt
	ds_read2_b32 v[16:17], v205 offset0:56 offset1:121
	v_lshl_add_u64 v[6:7], v[6:7], 0, v[90:91]
	ds_read2_b32 v[18:19], v205 offset0:186 offset1:251
	ds_read2_b32 v[20:21], v0 offset0:60 offset1:125
	ds_read2_b32 v[8:9], v0 offset0:190 offset1:255
	s_waitcnt lgkmcnt(0)
	v_cvt_pk_bf16_f32 v12, v16, v17
	v_cvt_pk_bf16_f32 v13, v18, v19
	v_cvt_pk_bf16_f32 v14, v20, v21
	v_cvt_pk_bf16_f32 v15, v8, v9
	global_store_dwordx4 v[6:7], v[12:15], off nt
	s_waitcnt lgkmcnt(0)
	v_pk_add_f32 v[34:35], v[134:135], v[34:35]
	s_mov_b64 s[40:41], 0
	v_pk_add_f32 v[34:35], v[136:137], v[34:35]

.LBB0_1104:
	s_add_i32 s10, s26, s59
	s_lshl_b64 s[40:41], s[8:9], 27
	s_add_u32 s7, s70, s40
	s_mov_b32 s11, s9
	s_addc_u32 s40, s2, s41
	s_waitcnt lgkmcnt(0)
	s_lshl_b64 s[10:11], s[10:11], 1
	s_add_u32 s10, s7, s10
	s_addc_u32 s11, s40, s11
	v_lshlrev_b32_e32 v0, 1, v68
	ds_read2_b32 v[16:17], v205 offset1:65
	v_lshl_add_u64 v[6:7], s[10:11], 0, v[0:1]
	ds_read2_b32 v[18:19], v205 offset0:130 offset1:195
	v_add_u32_e32 v0, 0x400, v205
	ds_read2_b32 v[20:21], v0 offset0:4 offset1:69
	ds_read2_b32 v[8:9], v0 offset0:134 offset1:199
	s_waitcnt lgkmcnt(0)
	v_cvt_pk_bf16_f32 v12, v16, v17
	v_cvt_pk_bf16_f32 v13, v18, v19
	v_cvt_pk_bf16_f32 v14, v20, v21
	v_cvt_pk_bf16_f32 v15, v8, v9
	v_add_u32_e32 v8, s42, v75
	v_ashrrev_i32_e32 v9, 31, v8
	v_lshlrev_b64 v[8:9], 13, v[8:9]
	v_lshl_add_u64 v[8:9], v[6:7], 0, v[8:9]
	global_store_dwordx4 v[8:9], v[12:15], off nt
	ds_read2_b32 v[16:17], v205 offset0:8 offset1:73
	ds_read2_b32 v[18:19], v205 offset0:138 offset1:203
	ds_read2_b32 v[20:21], v0 offset0:12 offset1:77
	ds_read2_b32 v[8:9], v0 offset0:142 offset1:207
	s_waitcnt lgkmcnt(0)
	v_cvt_pk_bf16_f32 v12, v16, v17
	v_cvt_pk_bf16_f32 v13, v18, v19
	v_cvt_pk_bf16_f32 v14, v20, v21
	v_cvt_pk_bf16_f32 v15, v8, v9
	v_add_u32_e32 v8, s42, v214
	v_ashrrev_i32_e32 v9, 31, v8
	v_lshlrev_b64 v[8:9], 13, v[8:9]
	v_lshl_add_u64 v[8:9], v[6:7], 0, v[8:9]
	global_store_dwordx4 v[8:9], v[12:15], off nt
	ds_read2_b32 v[16:17], v205 offset0:16 offset1:81
	ds_read2_b32 v[18:19], v205 offset0:146 offset1:211
	ds_read2_b32 v[20:21], v0 offset0:20 offset1:85
	ds_read2_b32 v[8:9], v0 offset0:150 offset1:215
	s_waitcnt lgkmcnt(0)
	v_cvt_pk_bf16_f32 v12, v16, v17
	v_cvt_pk_bf16_f32 v13, v18, v19
	v_cvt_pk_bf16_f32 v14, v20, v21
	v_cvt_pk_bf16_f32 v15, v8, v9
	v_add_u32_e32 v8, s42, v215
	v_ashrrev_i32_e32 v9, 31, v8
	v_lshlrev_b64 v[8:9], 13, v[8:9]
	v_lshl_add_u64 v[8:9], v[6:7], 0, v[8:9]
	global_store_dwordx4 v[8:9], v[12:15], off nt
	ds_read2_b32 v[16:17], v205 offset0:24 offset1:89
	ds_read2_b32 v[18:19], v205 offset0:154 offset1:219
	ds_read2_b32 v[20:21], v0 offset0:28 offset1:93
	ds_read2_b32 v[8:9], v0 offset0:158 offset1:223
	s_waitcnt lgkmcnt(0)
	v_cvt_pk_bf16_f32 v12, v16, v17
	v_cvt_pk_bf16_f32 v13, v18, v19
	v_cvt_pk_bf16_f32 v14, v20, v21
	v_cvt_pk_bf16_f32 v15, v8, v9
	v_add_u32_e32 v8, s42, v216
	v_ashrrev_i32_e32 v9, 31, v8
	v_lshlrev_b64 v[8:9], 13, v[8:9]
	v_lshl_add_u64 v[8:9], v[6:7], 0, v[8:9]
	global_store_dwordx4 v[8:9], v[12:15], off nt
	ds_read2_b32 v[16:17], v205 offset0:32 offset1:97
	ds_read2_b32 v[18:19], v205 offset0:162 offset1:227
	ds_read2_b32 v[20:21], v0 offset0:36 offset1:101
	ds_read2_b32 v[8:9], v0 offset0:166 offset1:231
	s_waitcnt lgkmcnt(0)
	v_cvt_pk_bf16_f32 v12, v16, v17
	v_cvt_pk_bf16_f32 v13, v18, v19
	v_cvt_pk_bf16_f32 v14, v20, v21
	v_cvt_pk_bf16_f32 v15, v8, v9
	v_add_u32_e32 v8, s42, v217
	v_ashrrev_i32_e32 v9, 31, v8
	v_lshlrev_b64 v[8:9], 13, v[8:9]
	v_lshl_add_u64 v[8:9], v[6:7], 0, v[8:9]
	global_store_dwordx4 v[8:9], v[12:15], off nt
	ds_read2_b32 v[16:17], v205 offset0:40 offset1:105
	ds_read2_b32 v[18:19], v205 offset0:170 offset1:235
	ds_read2_b32 v[20:21], v0 offset0:44 offset1:109
	ds_read2_b32 v[8:9], v0 offset0:174 offset1:239
	s_waitcnt lgkmcnt(0)
	v_cvt_pk_bf16_f32 v12, v16, v17
	v_cvt_pk_bf16_f32 v13, v18, v19
	v_cvt_pk_bf16_f32 v14, v20, v21
	v_cvt_pk_bf16_f32 v15, v8, v9
	v_add_u32_e32 v8, s42, v218
	v_ashrrev_i32_e32 v9, 31, v8
	v_lshlrev_b64 v[8:9], 13, v[8:9]
	v_lshl_add_u64 v[8:9], v[6:7], 0, v[8:9]
	global_store_dwordx4 v[8:9], v[12:15], off nt
	ds_read2_b32 v[16:17], v205 offset0:48 offset1:113
	ds_read2_b32 v[18:19], v205 offset0:178 offset1:243
	ds_read2_b32 v[20:21], v0 offset0:52 offset1:117
	ds_read2_b32 v[8:9], v0 offset0:182 offset1:247
	s_waitcnt lgkmcnt(0)
	v_cvt_pk_bf16_f32 v12, v16, v17
	v_cvt_pk_bf16_f32 v13, v18, v19
	v_cvt_pk_bf16_f32 v14, v20, v21
	v_cvt_pk_bf16_f32 v15, v8, v9
	v_add_u32_e32 v8, s42, v219
	v_ashrrev_i32_e32 v9, 31, v8
	v_lshlrev_b64 v[8:9], 13, v[8:9]
	v_lshl_add_u64 v[8:9], v[6:7], 0, v[8:9]
	global_store_dwordx4 v[8:9], v[12:15], off nt
	ds_read2_b32 v[16:17], v205 offset0:56 offset1:121
	ds_read2_b32 v[18:19], v205 offset0:186 offset1:251
	ds_read2_b32 v[20:21], v0 offset0:60 offset1:125
	ds_read2_b32 v[8:9], v0 offset0:190 offset1:255
	s_waitcnt lgkmcnt(0)
	v_cvt_pk_bf16_f32 v12, v16, v17
	v_cvt_pk_bf16_f32 v13, v18, v19
	v_cvt_pk_bf16_f32 v14, v20, v21
	v_cvt_pk_bf16_f32 v15, v8, v9
	v_add_u32_e32 v8, s42, v220
	v_ashrrev_i32_e32 v9, 31, v8
	v_lshlrev_b64 v[8:9], 13, v[8:9]
	v_lshl_add_u64 v[6:7], v[6:7], 0, v[8:9]
	global_store_dwordx4 v[6:7], v[12:15], off nt
	s_waitcnt lgkmcnt(0)

.LBB0_1333:
	s_add_i32 s10, s26, s58
	s_mul_i32 s11, s8, 0x1400000
	s_mul_hi_u32 s7, s8, 0x1400000
	s_add_u32 s41, s17, s11
	s_addc_u32 s7, s12, s7
	s_ashr_i32 s11, s10, 31
	s_waitcnt lgkmcnt(0)
	s_lshl_b64 s[10:11], s[10:11], 1
	s_add_u32 s10, s41, s10
	s_addc_u32 s11, s7, s11
	v_lshlrev_b32_e32 v0, 1, v68
	ds_read2_b32 v[16:17], v205 offset1:65
	v_lshl_add_u64 v[6:7], s[10:11], 0, v[0:1]
	ds_read2_b32 v[18:19], v205 offset0:130 offset1:195
	v_add_u32_e32 v0, 0x400, v205
	ds_read2_b32 v[20:21], v0 offset0:4 offset1:69
	ds_read2_b32 v[8:9], v0 offset0:134 offset1:199
	s_waitcnt lgkmcnt(0)
	v_cvt_pk_bf16_f32 v12, v16, v17
	v_cvt_pk_bf16_f32 v13, v18, v19
	v_cvt_pk_bf16_f32 v14, v20, v21
	v_cvt_pk_bf16_f32 v15, v8, v9
	v_add_u32_e32 v8, s40, v75
	v_ashrrev_i32_e32 v9, 31, v8
	v_lshlrev_b64 v[8:9], 13, v[8:9]
	v_lshl_add_u64 v[8:9], v[6:7], 0, v[8:9]
	global_store_dwordx4 v[8:9], v[12:15], off nt
	ds_read2_b32 v[16:17], v205 offset0:8 offset1:73
	ds_read2_b32 v[18:19], v205 offset0:138 offset1:203
	ds_read2_b32 v[20:21], v0 offset0:12 offset1:77
	ds_read2_b32 v[8:9], v0 offset0:142 offset1:207
	s_waitcnt lgkmcnt(0)
	v_cvt_pk_bf16_f32 v12, v16, v17
	v_cvt_pk_bf16_f32 v13, v18, v19
	v_cvt_pk_bf16_f32 v14, v20, v21
	v_cvt_pk_bf16_f32 v15, v8, v9
	v_add_u32_e32 v8, s40, v214
	v_ashrrev_i32_e32 v9, 31, v8
	v_lshlrev_b64 v[8:9], 13, v[8:9]
	v_lshl_add_u64 v[8:9], v[6:7], 0, v[8:9]
	global_store_dwordx4 v[8:9], v[12:15], off nt
	ds_read2_b32 v[16:17], v205 offset0:16 offset1:81
	ds_read2_b32 v[18:19], v205 offset0:146 offset1:211
	ds_read2_b32 v[20:21], v0 offset0:20 offset1:85
	ds_read2_b32 v[8:9], v0 offset0:150 offset1:215
	s_waitcnt lgkmcnt(0)
	v_cvt_pk_bf16_f32 v12, v16, v17
	v_cvt_pk_bf16_f32 v13, v18, v19
	v_cvt_pk_bf16_f32 v14, v20, v21
	v_cvt_pk_bf16_f32 v15, v8, v9
	v_add_u32_e32 v8, s40, v215
	v_ashrrev_i32_e32 v9, 31, v8
	v_lshlrev_b64 v[8:9], 13, v[8:9]
	v_lshl_add_u64 v[8:9], v[6:7], 0, v[8:9]
	global_store_dwordx4 v[8:9], v[12:15], off nt
	ds_read2_b32 v[16:17], v205 offset0:24 offset1:89
	ds_read2_b32 v[18:19], v205 offset0:154 offset1:219
	ds_read2_b32 v[20:21], v0 offset0:28 offset1:93
	ds_read2_b32 v[8:9], v0 offset0:158 offset1:223
	s_waitcnt lgkmcnt(0)
	v_cvt_pk_bf16_f32 v12, v16, v17
	v_cvt_pk_bf16_f32 v13, v18, v19
	v_cvt_pk_bf16_f32 v14, v20, v21
	v_cvt_pk_bf16_f32 v15, v8, v9
	v_add_u32_e32 v8, s40, v216
	v_ashrrev_i32_e32 v9, 31, v8
	v_lshlrev_b64 v[8:9], 13, v[8:9]
	v_lshl_add_u64 v[8:9], v[6:7], 0, v[8:9]
	global_store_dwordx4 v[8:9], v[12:15], off nt
	ds_read2_b32 v[16:17], v205 offset0:32 offset1:97
	ds_read2_b32 v[18:19], v205 offset0:162 offset1:227
	ds_read2_b32 v[20:21], v0 offset0:36 offset1:101
	ds_read2_b32 v[8:9], v0 offset0:166 offset1:231
	s_waitcnt lgkmcnt(0)
	v_cvt_pk_bf16_f32 v12, v16, v17
	v_cvt_pk_bf16_f32 v13, v18, v19
	v_cvt_pk_bf16_f32 v14, v20, v21
	v_cvt_pk_bf16_f32 v15, v8, v9
	v_add_u32_e32 v8, s40, v217
	v_ashrrev_i32_e32 v9, 31, v8
	v_lshlrev_b64 v[8:9], 13, v[8:9]
	v_lshl_add_u64 v[8:9], v[6:7], 0, v[8:9]
	global_store_dwordx4 v[8:9], v[12:15], off nt
	ds_read2_b32 v[16:17], v205 offset0:40 offset1:105
	ds_read2_b32 v[18:19], v205 offset0:170 offset1:235
	ds_read2_b32 v[20:21], v0 offset0:44 offset1:109
	ds_read2_b32 v[8:9], v0 offset0:174 offset1:239
	s_waitcnt lgkmcnt(0)
	v_cvt_pk_bf16_f32 v12, v16, v17
	v_cvt_pk_bf16_f32 v13, v18, v19
	v_cvt_pk_bf16_f32 v14, v20, v21
	v_cvt_pk_bf16_f32 v15, v8, v9
	v_add_u32_e32 v8, s40, v218
	v_ashrrev_i32_e32 v9, 31, v8
	v_lshlrev_b64 v[8:9], 13, v[8:9]
	v_lshl_add_u64 v[8:9], v[6:7], 0, v[8:9]
	global_store_dwordx4 v[8:9], v[12:15], off nt
	ds_read2_b32 v[16:17], v205 offset0:48 offset1:113
	ds_read2_b32 v[18:19], v205 offset0:178 offset1:243
	ds_read2_b32 v[20:21], v0 offset0:52 offset1:117
	ds_read2_b32 v[8:9], v0 offset0:182 offset1:247
	s_waitcnt lgkmcnt(0)
	v_cvt_pk_bf16_f32 v12, v16, v17
	v_cvt_pk_bf16_f32 v13, v18, v19
	v_cvt_pk_bf16_f32 v14, v20, v21
	v_cvt_pk_bf16_f32 v15, v8, v9
	v_add_u32_e32 v8, s40, v219
	v_ashrrev_i32_e32 v9, 31, v8
	v_lshlrev_b64 v[8:9], 13, v[8:9]
	v_lshl_add_u64 v[8:9], v[6:7], 0, v[8:9]
	global_store_dwordx4 v[8:9], v[12:15], off nt
	ds_read2_b32 v[16:17], v205 offset0:56 offset1:121
	ds_read2_b32 v[18:19], v205 offset0:186 offset1:251
	ds_read2_b32 v[20:21], v0 offset0:60 offset1:125
	ds_read2_b32 v[8:9], v0 offset0:190 offset1:255
	s_waitcnt lgkmcnt(0)
	v_cvt_pk_bf16_f32 v12, v16, v17
	v_cvt_pk_bf16_f32 v13, v18, v19
	v_cvt_pk_bf16_f32 v14, v20, v21
	v_cvt_pk_bf16_f32 v15, v8, v9
	v_add_u32_e32 v8, s40, v220
	v_ashrrev_i32_e32 v9, 31, v8
	v_lshlrev_b64 v[8:9], 13, v[8:9]
	v_lshl_add_u64 v[6:7], v[6:7], 0, v[8:9]
	global_store_dwordx4 v[6:7], v[12:15], off nt
	s_waitcnt lgkmcnt(0)
	s_mov_b64 s[40:41], 0
